# speedup vs baseline: 1.0073x; 1.0073x over previous
.LBB1_34:
	s_or_b64 exec, exec, s[6:7]
	v_or_b32_e32 v14, 0x400, v244
	s_movk_i32 s6, 0x680
	v_cmp_gt_u32_e64 s[6:7], s6, v14
	v_mov_b32_e32 v133, 0
	v_mov_b32_e32 v134, 0
	v_mov_b32_e32 v135, 0
	s_and_saveexec_b64 s[8:9], s[6:7]
	s_cbranch_execz .LBB1_36
	v_lshlrev_b32_e32 v0, 4, v14
	global_load_dwordx4 v[132:135], v0, s[2:3]
.LBB1_36:
	s_or_b64 exec, exec, s[8:9]
	s_movk_i32 s2, 0x180
	v_cmp_gt_u32_e64 s[8:9], s2, v244
	v_mov_b32_e32 v136, 0
	v_mov_b32_e32 v140, 0
	v_mov_b32_e32 v141, 0
	v_mov_b32_e32 v142, 0
	v_mov_b32_e32 v143, 0
	s_and_saveexec_b64 s[2:3], s[8:9]
	s_cbranch_execz .LBB1_38
	v_add_co_u32_e32 v0, vcc, 0x5000, v126
	s_nop 1
	v_addc_co_u32_e32 v1, vcc, 0, v127, vcc
	global_load_dwordx4 v[140:143], v[0:1], off

.LBB1_59:
	ds_write_b128 v124, v[132:135] offset:51216
	s_or_b64 exec, exec, s[2:3]
	s_and_saveexec_b64 s[2:3], s[8:9]
	s_cbranch_execz .LBB1_43

.LBB1_63:
	s_or_b64 exec, exec, s[6:7]
	s_load_dwordx4 s[4:7], s[0:1], 0x78
	v_lshrrev_b32_e32 v111, 2, v244
	v_lshlrev_b32_e32 v113, 4, v170
	v_and_b32_e32 v181, 12, v111
	v_or_b32_e32 v1, v113, v181
	v_lshlrev_b32_e32 v1, 2, v1
	v_or_b32_e32 v175, v113, v183
	s_waitcnt lgkmcnt(0)
	s_barrier
	v_mov_b32_e32 v0, 0
	v_lshlrev_b32_e32 v110, 2, v175
	global_load_dwordx4 a[138:141], v1, s[4:5]
	global_load_dword v112, v110, s[4:5]
	global_load_dword a142, v0, s[6:7]
	ds_read_b64 v[0:1], v0 offset:34816
	s_waitcnt lgkmcnt(0)
	v_readfirstlane_b32 s6, v0
	v_readfirstlane_b32 s7, v1
	s_and_saveexec_b64 s[4:5], s[12:13]
	s_cbranch_execz .LBB1_70
	v_cmp_eq_u32_e32 vcc, 12, v183
	ds_read_b128 v[144:147], v124 offset:34832
	ds_read_b128 v[148:151], v124 offset:48144
	ds_read_b128 v[152:155], v124 offset:35856
	ds_read_b128 v[156:159], v124 offset:49168
	v_mov_b32_e32 v14, v119
	v_lshrrev_b32_e32 v114, 4, v244
	v_cndmask_b32_e64 v0, 0, 1.0, vcc
	v_pk_add_f32 v[2:3], v[0:1], v[6:7] op_sel_hi:[0,1]
	v_cvt_pk_f16_f32 v6, v2, v3
	v_pk_add_f32 v[2:3], v[0:1], v[8:9] op_sel_hi:[0,1]
	v_cvt_pk_f16_f32 v7, v2, v3
	v_pk_add_f32 v[2:3], v[0:1], v[10:11] op_sel_hi:[0,1]
	v_cvt_pk_f16_f32 v8, v2, v3
	v_pk_add_f32 v[2:3], v[0:1], v[12:13] op_sel_hi:[0,1]
	v_cvt_pk_f16_f32 v9, v2, v3
	v_pk_add_f32 v[2:3], v[0:1], v[14:15] op_sel_hi:[0,1]
	s_nop 0
	s_waitcnt lgkmcnt(3)
	v_mfma_f32_16x16x32_f16 a[0:3], v[6:9], v[144:147], 0
	ds_read_b128 v[144:147], v124 offset:36880
	s_movk_i32 s2, 0x190
	s_nop 0
	s_waitcnt lgkmcnt(3)
	v_mfma_f32_16x16x32_f16 a[4:7], v[6:9], v[148:151], 0
	ds_read_b128 v[148:151], v124 offset:50192
	v_cvt_pk_f16_f32 v6, v2, v3
	v_pk_add_f32 v[2:3], v[0:1], v[16:17] op_sel_hi:[0,1]
	v_cvt_pk_f16_f32 v7, v2, v3
	v_pk_add_f32 v[2:3], v[0:1], v[18:19] op_sel_hi:[0,1]
	v_cvt_pk_f16_f32 v8, v2, v3
	v_pk_add_f32 v[2:3], v[0:1], v[20:21] op_sel_hi:[0,1]
	v_cvt_pk_f16_f32 v9, v2, v3
	s_nop 0
	s_waitcnt lgkmcnt(3)
	v_mfma_f32_16x16x32_f16 a[0:3], v[6:9], v[152:155], a[0:3]
	ds_read_b128 v[152:155], v124 offset:37904
	v_pk_add_f32 v[2:3], v[0:1], v[26:27] op_sel_hi:[0,1]
	s_nop 0
	s_waitcnt lgkmcnt(3)
	v_mfma_f32_16x16x32_f16 a[4:7], v[6:9], v[156:159], a[4:7]
	ds_read_b128 v[156:159], v124 offset:51216
	v_cvt_pk_f16_f32 v6, v2, v3
	v_pk_add_f32 v[2:3], v[0:1], v[28:29] op_sel_hi:[0,1]
	v_cvt_pk_f16_f32 v7, v2, v3
	v_pk_add_f32 v[2:3], v[0:1], v[30:31] op_sel_hi:[0,1]
	v_cvt_pk_f16_f32 v8, v2, v3
	v_pk_add_f32 v[2:3], v[0:1], v[32:33] op_sel_hi:[0,1]
	v_cvt_pk_f16_f32 v9, v2, v3
	v_pk_add_f32 v[2:3], v[0:1], v[22:23] op_sel_hi:[0,1]
	s_nop 0
	s_waitcnt lgkmcnt(3)
	v_mfma_f32_16x16x32_f16 a[0:3], v[6:9], v[144:147], a[0:3]
	ds_read_b128 v[144:147], v124 offset:38928
	s_nop 0
	s_waitcnt lgkmcnt(3)
	v_mfma_f32_16x16x32_f16 a[4:7], v[6:9], v[148:151], a[4:7]
	ds_read_b128 v[148:151], v124 offset:52240
	v_cvt_pk_f16_f32 v6, v2, v3
	v_pk_add_f32 v[2:3], v[0:1], v[24:25] op_sel_hi:[0,1]
	v_cvt_pk_f16_f32 v7, v2, v3
	v_pk_add_f32 v[2:3], v[0:1], v[34:35] op_sel_hi:[0,1]
	v_cvt_pk_f16_f32 v8, v2, v3
	v_pk_add_f32 v[2:3], v[0:1], v[36:37] op_sel_hi:[0,1]
	v_cvt_pk_f16_f32 v9, v2, v3
	v_pk_add_f32 v[2:3], v[0:1], v[42:43] op_sel_hi:[0,1]
	s_nop 0
	s_waitcnt lgkmcnt(3)
	v_mfma_f32_16x16x32_f16 a[0:3], v[6:9], v[152:155], a[0:3]
	ds_read_b128 v[152:155], v124 offset:39952
	s_nop 0
	s_waitcnt lgkmcnt(3)
	v_mfma_f32_16x16x32_f16 a[4:7], v[6:9], v[156:159], a[4:7]
	ds_read_b128 v[156:159], v124 offset:53264
	v_cvt_pk_f16_f32 v6, v2, v3
	v_pk_add_f32 v[2:3], v[0:1], v[44:45] op_sel_hi:[0,1]
	v_cvt_pk_f16_f32 v7, v2, v3
	v_pk_add_f32 v[2:3], v[0:1], v[46:47] op_sel_hi:[0,1]
	v_cvt_pk_f16_f32 v8, v2, v3
	v_pk_add_f32 v[2:3], v[0:1], v[48:49] op_sel_hi:[0,1]
	v_cvt_pk_f16_f32 v9, v2, v3
	v_pk_add_f32 v[2:3], v[0:1], v[38:39] op_sel_hi:[0,1]
	s_nop 0
	s_waitcnt lgkmcnt(3)
	v_mfma_f32_16x16x32_f16 a[0:3], v[6:9], v[144:147], a[0:3]
	ds_read_b128 v[144:147], v124 offset:40976
	s_nop 0
	s_waitcnt lgkmcnt(3)
	v_mfma_f32_16x16x32_f16 a[4:7], v[6:9], v[148:151], a[4:7]
	ds_read_b128 v[148:151], v124 offset:54288
	v_cvt_pk_f16_f32 v6, v2, v3
	v_pk_add_f32 v[2:3], v[0:1], v[40:41] op_sel_hi:[0,1]
	v_cvt_pk_f16_f32 v7, v2, v3
	v_pk_add_f32 v[2:3], v[0:1], v[50:51] op_sel_hi:[0,1]
	v_cvt_pk_f16_f32 v8, v2, v3
	v_pk_add_f32 v[2:3], v[0:1], v[52:53] op_sel_hi:[0,1]
	v_cvt_pk_f16_f32 v9, v2, v3
	v_pk_add_f32 v[2:3], v[0:1], v[58:59] op_sel_hi:[0,1]
	s_nop 0
	s_waitcnt lgkmcnt(3)
	v_mfma_f32_16x16x32_f16 a[0:3], v[6:9], v[152:155], a[0:3]
	ds_read_b128 v[152:155], v124 offset:42000
	s_nop 0
	s_waitcnt lgkmcnt(3)
	v_mfma_f32_16x16x32_f16 a[4:7], v[6:9], v[156:159], a[4:7]
	ds_read_b128 v[156:159], v124 offset:55312
	v_cvt_pk_f16_f32 v6, v2, v3
	v_pk_add_f32 v[2:3], v[0:1], v[60:61] op_sel_hi:[0,1]
	v_cvt_pk_f16_f32 v7, v2, v3
	v_pk_add_f32 v[2:3], v[0:1], v[62:63] op_sel_hi:[0,1]
	v_cvt_pk_f16_f32 v8, v2, v3
	v_pk_add_f32 v[2:3], v[0:1], v[64:65] op_sel_hi:[0,1]
	v_cvt_pk_f16_f32 v9, v2, v3
	v_pk_add_f32 v[2:3], v[0:1], v[54:55] op_sel_hi:[0,1]
	s_nop 0
	s_waitcnt lgkmcnt(3)
	v_mfma_f32_16x16x32_f16 a[0:3], v[6:9], v[144:147], a[0:3]
	ds_read_b128 v[144:147], v124 offset:43024
	s_nop 0
	s_waitcnt lgkmcnt(3)
	v_mfma_f32_16x16x32_f16 a[4:7], v[6:9], v[148:151], a[4:7]
	ds_read_b128 v[148:151], v124 offset:56336
	v_cvt_pk_f16_f32 v6, v2, v3
	v_pk_add_f32 v[2:3], v[0:1], v[56:57] op_sel_hi:[0,1]
	v_cvt_pk_f16_f32 v7, v2, v3
	v_pk_add_f32 v[2:3], v[0:1], v[66:67] op_sel_hi:[0,1]
	v_cvt_pk_f16_f32 v8, v2, v3
	v_pk_add_f32 v[2:3], v[0:1], v[68:69] op_sel_hi:[0,1]
	v_cvt_pk_f16_f32 v9, v2, v3
	v_pk_add_f32 v[2:3], v[0:1], v[74:75] op_sel_hi:[0,1]
	s_nop 0
	s_waitcnt lgkmcnt(3)
	v_mfma_f32_16x16x32_f16 a[0:3], v[6:9], v[152:155], a[0:3]
	ds_read_b128 v[152:155], v124 offset:44048
	s_nop 0
	s_waitcnt lgkmcnt(3)
	v_mfma_f32_16x16x32_f16 a[4:7], v[6:9], v[156:159], a[4:7]
	ds_read_b128 v[156:159], v124 offset:57360
	v_cvt_pk_f16_f32 v6, v2, v3
	v_pk_add_f32 v[2:3], v[0:1], v[76:77] op_sel_hi:[0,1]
	v_cvt_pk_f16_f32 v7, v2, v3
	v_pk_add_f32 v[2:3], v[0:1], v[78:79] op_sel_hi:[0,1]
	v_cvt_pk_f16_f32 v8, v2, v3
	v_pk_add_f32 v[2:3], v[0:1], v[80:81] op_sel_hi:[0,1]
	v_cvt_pk_f16_f32 v9, v2, v3
	v_pk_add_f32 v[2:3], v[0:1], v[70:71] op_sel_hi:[0,1]
	s_nop 0
	s_waitcnt lgkmcnt(3)
	v_mfma_f32_16x16x32_f16 a[0:3], v[6:9], v[144:147], a[0:3]
	ds_read_b128 v[144:147], v124 offset:45072
	s_nop 0
	s_waitcnt lgkmcnt(3)
	v_mfma_f32_16x16x32_f16 a[4:7], v[6:9], v[148:151], a[4:7]
	ds_read_b128 v[148:151], v124 offset:58384
	v_cvt_pk_f16_f32 v6, v2, v3
	v_pk_add_f32 v[2:3], v[0:1], v[72:73] op_sel_hi:[0,1]
	v_cvt_pk_f16_f32 v7, v2, v3
	v_pk_add_f32 v[2:3], v[0:1], v[82:83] op_sel_hi:[0,1]
	v_cvt_pk_f16_f32 v8, v2, v3
	v_pk_add_f32 v[2:3], v[0:1], v[84:85] op_sel_hi:[0,1]
	v_cvt_pk_f16_f32 v9, v2, v3
	v_pk_add_f32 v[2:3], v[0:1], v[90:91] op_sel_hi:[0,1]
	s_nop 0
	s_waitcnt lgkmcnt(3)
	v_mfma_f32_16x16x32_f16 a[0:3], v[6:9], v[152:155], a[0:3]
	ds_read_b128 v[152:155], v124 offset:46096
	s_nop 0
	s_waitcnt lgkmcnt(3)
	v_mfma_f32_16x16x32_f16 a[4:7], v[6:9], v[156:159], a[4:7]
	ds_read_b128 v[156:159], v124 offset:59408
	v_cvt_pk_f16_f32 v6, v2, v3
	v_pk_add_f32 v[2:3], v[0:1], v[92:93] op_sel_hi:[0,1]
	v_cvt_pk_f16_f32 v7, v2, v3
	v_pk_add_f32 v[2:3], v[0:1], v[94:95] op_sel_hi:[0,1]
	v_cvt_pk_f16_f32 v8, v2, v3
	v_pk_add_f32 v[2:3], v[0:1], v[96:97] op_sel_hi:[0,1]
	v_cvt_pk_f16_f32 v9, v2, v3
	v_pk_add_f32 v[2:3], v[0:1], v[86:87] op_sel_hi:[0,1]
	s_nop 0
	s_waitcnt lgkmcnt(3)
	v_mfma_f32_16x16x32_f16 a[0:3], v[6:9], v[144:147], a[0:3]
	ds_read_b128 v[144:147], v124 offset:47120
	s_nop 0
	s_waitcnt lgkmcnt(3)
	v_mfma_f32_16x16x32_f16 a[4:7], v[6:9], v[148:151], a[4:7]
	ds_read_b128 v[148:151], v124 offset:60432
	v_cvt_pk_f16_f32 v6, v2, v3
	v_pk_add_f32 v[2:3], v[0:1], v[88:89] op_sel_hi:[0,1]
	v_cvt_pk_f16_f32 v7, v2, v3
	v_pk_add_f32 v[2:3], v[0:1], v[98:99] op_sel_hi:[0,1]
	v_pk_add_f32 v[0:1], v[0:1], v[100:101] op_sel_hi:[0,1]
	v_cvt_pk_f16_f32 v8, v2, v3
	v_cvt_pk_f16_f32 v9, v0, v1
	v_mov_b32_e32 v0, 0x180
	s_nop 0
	s_waitcnt lgkmcnt(3)
	v_mfma_f32_16x16x32_f16 a[128:131], v[6:9], v[152:155], a[0:3]
	v_lshl_or_b32 v0, v114, 3, v0
	v_cmp_gt_u32_e64 s[2:3], s2, v0
	s_and_b64 s[2:3], vcc, s[2:3]
	s_nop 0
	s_waitcnt lgkmcnt(2)
	v_mfma_f32_16x16x32_f16 a[0:3], v[6:9], v[156:159], a[4:7]
	v_cndmask_b32_e64 v0, 0, 1.0, s[2:3]
	v_pk_add_f32 v[2:3], v[0:1], v[106:107] op_sel_hi:[0,1]
	v_cvt_pk_f16_f32 v6, v2, v3
	v_pk_add_f32 v[2:3], v[0:1], v[108:109] op_sel_hi:[0,1]
	v_cvt_pk_f16_f32 v7, v2, v3
	v_pk_add_f32 v[2:3], v[0:1], v[102:103] op_sel_hi:[0,1]
	v_pk_add_f32 v[0:1], v[0:1], v[104:105] op_sel_hi:[0,1]
	v_cvt_pk_f16_f32 v8, v2, v3
	v_cvt_pk_f16_f32 v9, v0, v1
	v_mov_b32_e32 v0, 0x27010
	s_nop 0
	s_waitcnt lgkmcnt(1)
	v_mfma_f32_16x16x32_f16 a[4:7], v[6:9], v[144:147], a[128:131]
	s_nop 0
	s_waitcnt lgkmcnt(0)
	v_mfma_f32_16x16x32_f16 a[0:3], v[6:9], v[148:151], a[0:3]
	s_nop 6
	v_accvgpr_read_b32 v13, a7
	v_accvgpr_read_b32 v10, a4
	v_lshlrev_b32_e32 v10, 2, v114
	v_or_b32_e32 v14, 1, v10
	v_accvgpr_read_b32 v12, a6
	v_accvgpr_read_b32 v11, a5
	v_cmp_gt_u32_e32 vcc, 13, v14
	v_accvgpr_read_b32 v9, a3
	v_accvgpr_read_b32 v6, a0
	v_lshl_add_u32 v6, v183, 2, v0
	v_accvgpr_read_b32 v8, a2
	v_accvgpr_read_b32 v7, a1
	v_lshl_add_u32 v0, v114, 9, v6
	ds_write_b32 v0, a4
	ds_write_b32 v0, a0 offset:64
	s_and_saveexec_b64 s[2:3], vcc
	v_lshl_add_u32 v0, v14, 7, v6
	ds_write2_b32 v0, v11, v7 offset1:16
	s_or_b64 exec, exec, s[2:3]
	v_or_b32_e32 v7, 2, v10
	v_cmp_gt_u32_e32 vcc, 13, v7
	s_and_saveexec_b64 s[2:3], vcc
	v_lshl_add_u32 v0, v7, 7, v6
	ds_write2_b32 v0, v12, v8 offset1:16
	s_or_b64 exec, exec, s[2:3]
	v_or_b32_e32 v7, 3, v10
	v_cmp_gt_u32_e32 vcc, 13, v7
	s_and_b64 exec, exec, vcc
	v_lshl_add_u32 v0, v7, 7, v6
	ds_write2_b32 v0, v13, v9 offset1:16
